# speedup vs baseline: 1.0184x; 1.0184x over previous
.LBB1_89:
	s_or_b64 exec, exec, s[16:17]
	s_add_i32 s41, s25, -12
	s_and_b64 s[16:17], s[18:19], exec
	s_cselect_b32 s26, s41, s25
	s_cmp_lg_u32 s26, 0
	s_cselect_b64 s[16:17], -1, 0
	s_cmp_eq_u32 s26, 0
	s_cselect_b64 s[38:39], -1, 0
	global_load_dword v7, v[168:169], off sc1
	v_add_u32_e32 v249, v61, v207
	ds_read_b128 v[64:67], v249
	ds_read_b128 v[68:71], v249 offset:64
	ds_read_b128 v[78:81], v249 offset:256
	ds_read_b128 v[82:85], v249 offset:320
	ds_read_b128 v[86:89], v249 offset:512
	ds_read_b128 v[90:93], v249 offset:576
	global_load_dword v8, v[168:169], off sc1
	s_waitcnt lgkmcnt(5)
	v_mfma_f32_16x16x32_f16 a[0:3], v[64:67], a[8:11], 0
	s_waitcnt lgkmcnt(4)
	v_mfma_f32_16x16x32_f16 a[0:3], v[68:71], a[12:15], a[0:3]
	s_waitcnt lgkmcnt(3)
	v_mfma_f32_16x16x32_f16 a[0:3], v[78:81], a[24:27], a[0:3]
	s_waitcnt lgkmcnt(2)
	v_mfma_f32_16x16x32_f16 a[0:3], v[82:85], a[28:31], a[0:3]
	s_waitcnt lgkmcnt(1)
	v_mfma_f32_16x16x32_f16 a[0:3], v[86:89], a[40:43], a[0:3]
	s_waitcnt lgkmcnt(0)
	v_mfma_f32_16x16x32_f16 a[4:7], v[90:93], a[44:47], a[0:3]
	v_mfma_f32_16x16x32_f16 a[0:3], v[64:67], a[16:19], 0
	v_mfma_f32_16x16x32_f16 a[0:3], v[68:71], a[20:23], a[0:3]
	v_mfma_f32_16x16x32_f16 a[0:3], v[78:81], a[32:35], a[0:3]
	v_mfma_f32_16x16x32_f16 a[0:3], v[82:85], a[36:39], a[0:3]
	v_mfma_f32_16x16x32_f16 a[0:3], v[86:89], a[48:51], a[0:3]
	v_mfma_f32_16x16x32_f16 a[0:3], v[90:93], a[52:55], a[0:3]
	global_load_dword v9, v[168:169], off sc1
	s_cmp_lt_u32 s25, 12
	s_cbranch_scc0 .Lpl0_loop
	s_waitcnt vmcnt(3) lgkmcnt(0)
	s_and_saveexec_b64 s[68:69], s[6:7]
	v_add_u32_e32 v0, 0x8400, v60
	ds_write2_b32 v0, v181, v184 offset1:16
	ds_write_b32 v60, v185 offset:33920
	s_mov_b64 exec, s[68:69]
	s_waitcnt lgkmcnt(0)
	s_barrier
.Lpl0_loop:
	s_waitcnt vmcnt(3)
	v_cmp_le_u32_e64 s[66:67], s71, v6
	s_cmp_eq_u64 s[66:67], exec
	s_cbranch_scc1 .Lpl0_done
	global_load_dword v6, v[168:169], off sc1
	s_waitcnt vmcnt(3)
	v_cmp_le_u32_e64 s[66:67], s71, v7
	s_cmp_eq_u64 s[66:67], exec
	s_cbranch_scc1 .Lpl0_done
	global_load_dword v7, v[168:169], off sc1
	s_waitcnt vmcnt(3)
	v_cmp_le_u32_e64 s[66:67], s71, v8
	s_cmp_eq_u64 s[66:67], exec
	s_cbranch_scc1 .Lpl0_done
	global_load_dword v8, v[168:169], off sc1
	s_waitcnt vmcnt(3)
	v_cmp_le_u32_e64 s[66:67], s71, v9
	s_cmp_eq_u64 s[66:67], exec
	s_cbranch_scc1 .Lpl0_done
	global_load_dword v9, v[168:169], off sc1
	s_add_i32 s65, s65, 1
	s_cmp_gt_u32 s65, 0xffff
	s_cbranch_scc0 .Lpl0_loop
.Lpl0_done:
.LBB1_87:
	s_cmp_lt_u32 s25, 12
	s_cbranch_scc0 .Lp0_pay
	buffer_load_dwordx4 v[54:57], v194, s[20:23], 0 offen sc1
	buffer_load_dwordx4 v[50:53], v195, s[20:23], 0 offen sc1
	buffer_load_dwordx4 v[46:49], v196, s[20:23], 0 offen sc1
	buffer_load_dwordx4 v[42:45], v197, s[20:23], 0 offen sc1
	buffer_load_dwordx4 v[38:41], v198, s[20:23], 0 offen sc1
	buffer_load_dwordx4 v[34:37], v199, s[20:23], 0 offen sc1
	s_branch .LBB1_106
